# P5 GLU epilogue: up-path clamp med3(U,-6,8) done by the [0,1] clamp modifier of the dequant pk_fma (U01 = clamp(acc*s/14 + (b+7)/14), U = 14*U01 - 6): one pk_fma per pair instead of two v_med3
# speedup vs baseline: 1.0061x; 1.0061x over previous
.LBB0_555:
	v_and_b32_e32 v6, 15, v4
	s_lshl_b32 s5, s5, 5
	v_lshlrev_b32_e32 v7, 7, v6
	s_and_b32 s5, s5, 0x60
	v_lshl_or_b32 v7, s22, 13, v7
	s_add_u32 s22, s44, 0x80
	v_or_b32_e32 v6, s5, v6
	s_waitcnt vmcnt(2)
	s_barrier
	s_addc_u32 s23, s45, 0
	s_add_i32 s55, s29, 0x18000
	s_mov_b32 m0, s55
	s_nop 0
	global_load_lds_dwordx4 v1, s[22:23] offset:0
	s_add_i32 s56, s29, 0x1a000
	s_mov_b32 m0, s56
	s_nop 0
	global_load_lds_dwordx4 v173, s[22:23] offset:0
	s_add_u32 s22, s18, 0x80
	s_addc_u32 s23, s19, 0
	s_add_i32 s57, s29, 0x8000
	s_mov_b32 m0, s57
	s_nop 0
	global_load_lds_dwordx4 v171, s[22:23] offset:0
	s_add_i32 s58, s29, 0xa000
	s_mov_b32 m0, s58
	s_nop 0
	global_load_lds_dwordx4 v174, s[22:23] offset:0
	s_add_u32 s24, s44, 0x20080
	s_addc_u32 s25, s45, 0
	s_add_i32 s59, s29, 0x1c000
	s_mov_b32 m0, s59
	s_nop 0
	global_load_lds_dwordx4 v1, s[24:25] offset:0
	s_add_i32 s60, s29, 0x1e000
	s_add_i32 s61, s29, 0xc000
	v_bfe_u32 v8, v4, 4, 2
	v_bfe_u32 v4, v4, 1, 3
	s_mov_b32 m0, s60
	s_nop 0
	global_load_lds_dwordx4 v173, s[24:25] offset:0
	s_add_u32 s24, s18, 0x380
	v_bitop3_b32 v5, v5, v4, 3 bitop3:0x6c
	v_bitop3_b32 v4, v8, v4, 4 bitop3:0x36
	s_addc_u32 s25, s19, 0
	v_lshlrev_b32_e32 v5, 4, v5
	v_lshlrev_b32_e32 v4, 4, v4
	v_lshlrev_b32_e32 v6, 7, v6
	s_cmpk_lt_u32 s4, 0x100
	v_and_b32_e32 v3, 0x1000, v3
	s_movk_i32 s4, 0x1f0
	v_or_b32_e32 v176, v6, v5
	v_or_b32_e32 v177, v6, v4
	s_waitcnt vmcnt(6)
	s_cselect_b64 s[26:27], -1, 0
	v_and_or_b32 v178, v2, s4, v3
	s_add_i32 s4, 0, 0x10000
	v_or_b32_e32 v9, v5, v7
	v_or_b32_e32 v7, v4, v7
	v_add_u32_e32 v179, s4, v176
	v_add_u32_e32 v180, s4, v177
	s_add_i32 s4, 0, 0x14000
	s_add_i32 s62, s29, 0xe000
	v_add_u32_e32 v181, s4, v176
	v_add_u32_e32 v182, s4, v177
	v_add_u32_e32 v183, 0, v9
	v_add_u32_e32 v184, 0, v7
	v_mov_b32_e32 v185, 0x7f7f7f7f
	s_movk_i32 s63, 0xffc0
	v_mov_b32_e32 v163, 0
	s_mov_b32 s96, 0xbf1d265f
	s_mov_b32 s98, 0xb99d265f
	s_mov_b32 s100, 0xc01d265f
	s_mov_b32 s74, 0x37124925
	s_mov_b32 s72, 0x3d924925
	s_mov_b32 s64, 0x41600000
	v_mov_b32_e32 v186, 0xc0c00000
	s_barrier
	s_branch .LBB0_558

.LBB0_566:
	s_lshl_b32 s35, s67, 10
	v_mov_b32_e32 v25, v0
	s_and_b32 s35, s35, 0x400
	s_add_i32 s35, s35, 0
	v_lshrrev_b32_e32 v26, 1, v25
	v_and_b32_e32 v162, 0x60, v26
	v_lshlrev_b32_e32 v3, 1, v25
	s_add_i32 s35, s35, 0x24cc0
	v_lshlrev_b32_e32 v2, 2, v162
	v_and_b32_e32 v3, 0x60, v3
	v_add3_u32 v14, s35, v2, v3
	ds_read_b128 v[2:5], v14
	ds_read_b128 v[6:9], v14 offset:512
	ds_read_b128 v[10:13], v14 offset:16
	v_ashrrev_i32_e32 v24, 2, v25
	s_lshl_b32 s35, s40, 10
	s_lshl_b32 s38, s38, 7
	s_waitcnt lgkmcnt(2)
	v_pk_mul_f32 v[16:17], v[4:5], s[100:101] op_sel_hi:[1,0]
	v_pk_mul_f32 v[18:19], v[2:3], s[100:101] op_sel_hi:[1,0]
	ds_read_b128 v[2:5], v14 offset:528
	s_waitcnt lgkmcnt(2)
	v_pk_fma_f32 v[20:21], v[8:9], s[72:73], 0.5 op_sel_hi:[1,0,0]
	s_waitcnt lgkmcnt(1)
	v_pk_mul_f32 v[8:9], v[12:13], s[100:101] op_sel_hi:[1,0]
	v_pk_fma_f32 v[22:23], v[6:7], s[72:73], 0.5 op_sel_hi:[1,0,0]
	v_and_b32_e32 v6, 16, v26
	s_waitcnt lgkmcnt(0)
	v_pk_fma_f32 v[14:15], v[2:3], s[72:73], 0.5 op_sel_hi:[1,0,0]
	v_and_b32_e32 v2, 15, v25
	v_pk_fma_f32 v[12:13], v[4:5], s[72:73], 0.5 op_sel_hi:[1,0,0]
	v_and_or_b32 v2, v24, s63, v2
	v_pk_fma_f32 v[4:5], v[158:159], s[98:99], v[18:19] op_sel_hi:[1,0,1]
	v_lshl_add_u32 v24, s37, 8, v2
	v_pk_fma_f32 v[2:3], v[160:161], s[98:99], v[16:17] op_sel_hi:[1,0,1]
	v_max_f32_e32 v4, 0xc1898193, v4
	v_max_f32_e32 v5, 0xc1898193, v5
	v_max_f32_e32 v30, 0xc1898193, v2
	v_max_f32_e32 v31, 0xc1898193, v3
	v_exp_f32_e32 v2, v4
	v_exp_f32_e32 v3, v5
	v_exp_f32_e32 v32, v30
	v_exp_f32_e32 v33, v31
	v_pk_fma_f32 v[2:3], v[2:3], s[96:97], s[96:97] op_sel_hi:[1,0,0]
	v_pk_fma_f32 v[28:29], v[154:155], s[74:75], v[22:23] op_sel_hi:[1,0,1] clamp
	v_rcp_f32_e32 v2, v2
	v_rcp_f32_e32 v3, v3
	v_pk_fma_f32 v[28:29], v[28:29], s[64:65], v[186:187] op_sel_hi:[1,0,0]
	v_pk_fma_f32 v[32:33], v[32:33], s[96:97], s[96:97] op_sel_hi:[1,0,0]
	v_pk_mul_f32 v[4:5], v[4:5], v[28:29]
	v_rcp_f32_e32 v32, v32
	v_rcp_f32_e32 v33, v33
	v_pk_mul_f32 v[4:5], v[4:5], v[2:3]
	v_pk_fma_f32 v[26:27], v[156:157], s[74:75], v[20:21] op_sel_hi:[1,0,1] clamp
	v_cvt_pk_fp8_f32 v2, v4, v5
	v_pk_fma_f32 v[26:27], v[26:27], s[64:65], v[186:187] op_sel_hi:[1,0,0]
	v_pk_mul_f32 v[4:5], v[30:31], v[26:27]
	v_pk_mul_f32 v[10:11], v[10:11], s[100:101] op_sel_hi:[1,0]
	v_pk_mul_f32 v[4:5], v[4:5], v[32:33]
	v_pk_fma_f32 v[26:27], v[150:151], s[98:99], v[10:11] op_sel_hi:[1,0,1]
	v_cvt_pk_fp8_f32 v2, v4, v5 op_sel:[0,0,1]
	v_pk_fma_f32 v[4:5], v[152:153], s[98:99], v[8:9] op_sel_hi:[1,0,1]
	v_max_f32_e32 v26, 0xc1898193, v26
	v_max_f32_e32 v4, 0xc1898193, v4
	v_max_f32_e32 v27, 0xc1898193, v27
	v_max_f32_e32 v5, 0xc1898193, v5
	v_pk_fma_f32 v[30:31], v[146:147], s[74:75], v[14:15] op_sel_hi:[1,0,1] clamp
	v_exp_f32_e32 v32, v26
	v_exp_f32_e32 v146, v4
	v_exp_f32_e32 v147, v5
	v_exp_f32_e32 v33, v27
	v_pk_fma_f32 v[30:31], v[30:31], s[64:65], v[186:187] op_sel_hi:[1,0,0]
	v_pk_fma_f32 v[146:147], v[146:147], s[96:97], s[96:97] op_sel_hi:[1,0,0]
	v_pk_fma_f32 v[32:33], v[32:33], s[96:97], s[96:97] op_sel_hi:[1,0,0]
	v_pk_mul_f32 v[26:27], v[26:27], v[30:31]
	v_rcp_f32_e32 v32, v32
	v_rcp_f32_e32 v33, v33
	v_rcp_f32_e32 v146, v146
	v_rcp_f32_e32 v147, v147
	v_pk_mul_f32 v[26:27], v[26:27], v[32:33]
	v_pk_fma_f32 v[28:29], v[148:149], s[74:75], v[12:13] op_sel_hi:[1,0,1] clamp
	v_cvt_pk_fp8_f32 v3, v26, v27
	v_pk_fma_f32 v[28:29], v[28:29], s[64:65], v[186:187] op_sel_hi:[1,0,0]
	v_pk_mul_f32 v[4:5], v[4:5], v[28:29]
	v_pk_fma_f32 v[26:27], v[142:143], s[98:99], v[18:19] op_sel_hi:[1,0,1]
	v_pk_mul_f32 v[4:5], v[4:5], v[146:147]
	v_max_f32_e32 v26, 0xc1898193, v26
	v_cvt_pk_fp8_f32 v3, v4, v5 op_sel:[0,0,1]
	v_pk_fma_f32 v[4:5], v[144:145], s[98:99], v[16:17] op_sel_hi:[1,0,1]
	v_max_f32_e32 v27, 0xc1898193, v27
	v_max_f32_e32 v32, 0xc1898193, v4
	v_max_f32_e32 v33, 0xc1898193, v5
	v_exp_f32_e32 v4, v26
	v_exp_f32_e32 v5, v27
	v_pk_fma_f32 v[30:31], v[138:139], s[74:75], v[22:23] op_sel_hi:[1,0,1] clamp
	v_exp_f32_e32 v138, v32
	v_exp_f32_e32 v139, v33
	v_pk_fma_f32 v[4:5], v[4:5], s[96:97], s[96:97] op_sel_hi:[1,0,0]
	v_pk_fma_f32 v[30:31], v[30:31], s[64:65], v[186:187] op_sel_hi:[1,0,0]
	v_rcp_f32_e32 v4, v4
	v_rcp_f32_e32 v5, v5
	v_pk_fma_f32 v[138:139], v[138:139], s[96:97], s[96:97] op_sel_hi:[1,0,0]
	v_pk_mul_f32 v[26:27], v[26:27], v[30:31]
	v_rcp_f32_e32 v138, v138
	v_rcp_f32_e32 v139, v139
	v_pk_mul_f32 v[26:27], v[26:27], v[4:5]
	v_pk_fma_f32 v[28:29], v[140:141], s[74:75], v[20:21] op_sel_hi:[1,0,1] clamp
	v_cvt_pk_fp8_f32 v4, v26, v27
	v_pk_fma_f32 v[28:29], v[28:29], s[64:65], v[186:187] op_sel_hi:[1,0,0]
	v_pk_mul_f32 v[26:27], v[32:33], v[28:29]
	v_pk_fma_f32 v[28:29], v[134:135], s[98:99], v[10:11] op_sel_hi:[1,0,1]
	v_pk_mul_f32 v[26:27], v[26:27], v[138:139]
	v_max_f32_e32 v28, 0xc1898193, v28
	v_cvt_pk_fp8_f32 v4, v26, v27 op_sel:[0,0,1]
	v_pk_fma_f32 v[26:27], v[136:137], s[98:99], v[8:9] op_sel_hi:[1,0,1]
	v_pk_fma_f32 v[32:33], v[130:131], s[74:75], v[14:15] op_sel_hi:[1,0,1] clamp
	v_max_f32_e32 v26, 0xc1898193, v26
	v_max_f32_e32 v29, 0xc1898193, v29
	v_max_f32_e32 v27, 0xc1898193, v27
	v_pk_fma_f32 v[30:31], v[132:133], s[74:75], v[12:13] op_sel_hi:[1,0,1] clamp
	v_exp_f32_e32 v130, v28
	v_exp_f32_e32 v132, v26
	v_exp_f32_e32 v133, v27
	v_exp_f32_e32 v131, v29
	v_pk_fma_f32 v[32:33], v[32:33], s[64:65], v[186:187] op_sel_hi:[1,0,0]
	v_pk_fma_f32 v[132:133], v[132:133], s[96:97], s[96:97] op_sel_hi:[1,0,0]
	v_pk_fma_f32 v[130:131], v[130:131], s[96:97], s[96:97] op_sel_hi:[1,0,0]
	v_pk_mul_f32 v[28:29], v[28:29], v[32:33]
	v_rcp_f32_e32 v130, v130
	v_rcp_f32_e32 v131, v131
	v_rcp_f32_e32 v132, v132
	v_rcp_f32_e32 v133, v133
	v_pk_mul_f32 v[28:29], v[28:29], v[130:131]
	v_pk_fma_f32 v[30:31], v[30:31], s[64:65], v[186:187] op_sel_hi:[1,0,0]
	v_cvt_pk_fp8_f32 v5, v28, v29
	v_pk_fma_f32 v[28:29], v[126:127], s[98:99], v[18:19] op_sel_hi:[1,0,1]
	v_max_f32_e32 v28, 0xc1898193, v28
	v_max_f32_e32 v29, 0xc1898193, v29
	v_pk_mul_f32 v[26:27], v[26:27], v[30:31]
	v_pk_fma_f32 v[32:33], v[122:123], s[74:75], v[22:23] op_sel_hi:[1,0,1] clamp
	v_pk_mul_f32 v[26:27], v[26:27], v[132:133]
	v_exp_f32_e32 v122, v28
	v_exp_f32_e32 v123, v29
	v_cvt_pk_fp8_f32 v5, v26, v27 op_sel:[0,0,1]
	v_pk_fma_f32 v[26:27], v[128:129], s[98:99], v[16:17] op_sel_hi:[1,0,1]
	v_pk_fma_f32 v[30:31], v[124:125], s[74:75], v[20:21] op_sel_hi:[1,0,1] clamp
	v_max_f32_e32 v26, 0xc1898193, v26
	v_max_f32_e32 v27, 0xc1898193, v27
	v_exp_f32_e32 v124, v26
	v_exp_f32_e32 v125, v27
	v_pk_fma_f32 v[122:123], v[122:123], s[96:97], s[96:97] op_sel_hi:[1,0,0]
	v_pk_fma_f32 v[32:33], v[32:33], s[64:65], v[186:187] op_sel_hi:[1,0,0]
	v_rcp_f32_e32 v122, v122
	v_rcp_f32_e32 v123, v123
	v_pk_fma_f32 v[124:125], v[124:125], s[96:97], s[96:97] op_sel_hi:[1,0,0]
	v_pk_mul_f32 v[28:29], v[28:29], v[32:33]
	v_rcp_f32_e32 v124, v124
	v_rcp_f32_e32 v125, v125
	v_pk_mul_f32 v[32:33], v[28:29], v[122:123]
	v_cvt_pk_fp8_f32 v28, v32, v33
	v_pk_fma_f32 v[30:31], v[30:31], s[64:65], v[186:187] op_sel_hi:[1,0,0]
	v_pk_mul_f32 v[26:27], v[26:27], v[30:31]
	v_pk_fma_f32 v[30:31], v[118:119], s[98:99], v[10:11] op_sel_hi:[1,0,1]
	v_pk_mul_f32 v[26:27], v[26:27], v[124:125]
	v_max_f32_e32 v30, 0xc1898193, v30
	v_cvt_pk_fp8_f32 v28, v26, v27 op_sel:[0,0,1]
	v_pk_fma_f32 v[26:27], v[120:121], s[98:99], v[8:9] op_sel_hi:[1,0,1]
	v_pk_fma_f32 v[32:33], v[116:117], s[74:75], v[12:13] op_sel_hi:[1,0,1] clamp
	v_max_f32_e32 v26, 0xc1898193, v26
	v_max_f32_e32 v31, 0xc1898193, v31
	v_max_f32_e32 v27, 0xc1898193, v27
	v_exp_f32_e32 v116, v30
	v_exp_f32_e32 v118, v26
	v_exp_f32_e32 v119, v27
	v_exp_f32_e32 v117, v31
	v_pk_fma_f32 v[114:115], v[114:115], s[74:75], v[14:15] op_sel_hi:[1,0,1] clamp
	v_pk_fma_f32 v[114:115], v[114:115], s[64:65], v[186:187] op_sel_hi:[1,0,0]
	v_pk_fma_f32 v[116:117], v[116:117], s[96:97], s[96:97] op_sel_hi:[1,0,0]
	v_rcp_f32_e32 v116, v116
	v_rcp_f32_e32 v117, v117
	v_pk_fma_f32 v[118:119], v[118:119], s[96:97], s[96:97] op_sel_hi:[1,0,0]
	v_pk_mul_f32 v[30:31], v[30:31], v[114:115]
	v_rcp_f32_e32 v118, v118
	v_rcp_f32_e32 v119, v119
	v_pk_mul_f32 v[30:31], v[30:31], v[116:117]
	v_pk_fma_f32 v[32:33], v[32:33], s[64:65], v[186:187] op_sel_hi:[1,0,0]
	v_cvt_pk_fp8_f32 v29, v30, v31
	v_pk_fma_f32 v[30:31], v[110:111], s[98:99], v[18:19] op_sel_hi:[1,0,1]
	v_max_f32_e32 v30, 0xc1898193, v30
	v_max_f32_e32 v31, 0xc1898193, v31
	v_pk_mul_f32 v[26:27], v[26:27], v[32:33]
	v_pk_fma_f32 v[32:33], v[108:109], s[74:75], v[20:21] op_sel_hi:[1,0,1] clamp
	v_pk_mul_f32 v[26:27], v[26:27], v[118:119]
	v_exp_f32_e32 v108, v30
	v_exp_f32_e32 v109, v31
	v_cvt_pk_fp8_f32 v29, v26, v27 op_sel:[0,0,1]
	v_pk_fma_f32 v[26:27], v[112:113], s[98:99], v[16:17] op_sel_hi:[1,0,1]
	v_pk_fma_f32 v[106:107], v[106:107], s[74:75], v[22:23] op_sel_hi:[1,0,1] clamp
	v_max_f32_e32 v26, 0xc1898193, v26
	v_max_f32_e32 v27, 0xc1898193, v27
	v_exp_f32_e32 v110, v26
	v_exp_f32_e32 v111, v27
	v_pk_fma_f32 v[108:109], v[108:109], s[96:97], s[96:97] op_sel_hi:[1,0,0]
	v_pk_fma_f32 v[106:107], v[106:107], s[64:65], v[186:187] op_sel_hi:[1,0,0]
	v_rcp_f32_e32 v108, v108
	v_rcp_f32_e32 v109, v109
	v_pk_fma_f32 v[110:111], v[110:111], s[96:97], s[96:97] op_sel_hi:[1,0,0]
	v_pk_mul_f32 v[30:31], v[30:31], v[106:107]
	v_rcp_f32_e32 v110, v110
	v_rcp_f32_e32 v111, v111
	v_pk_mul_f32 v[106:107], v[30:31], v[108:109]
	v_cvt_pk_fp8_f32 v30, v106, v107
	v_pk_fma_f32 v[32:33], v[32:33], s[64:65], v[186:187] op_sel_hi:[1,0,0]
	v_pk_mul_f32 v[26:27], v[26:27], v[32:33]
	v_pk_fma_f32 v[32:33], v[102:103], s[98:99], v[10:11] op_sel_hi:[1,0,1]
	v_pk_mul_f32 v[26:27], v[26:27], v[110:111]
	v_max_f32_e32 v32, 0xc1898193, v32
	v_cvt_pk_fp8_f32 v30, v26, v27 op_sel:[0,0,1]
	v_pk_fma_f32 v[26:27], v[104:105], s[98:99], v[8:9] op_sel_hi:[1,0,1]
	v_max_f32_e32 v33, 0xc1898193, v33
	v_max_f32_e32 v26, 0xc1898193, v26
	v_max_f32_e32 v27, 0xc1898193, v27
	v_exp_f32_e32 v102, v32
	v_exp_f32_e32 v104, v26
	v_exp_f32_e32 v105, v27
	v_exp_f32_e32 v103, v33
	v_pk_fma_f32 v[98:99], v[98:99], s[74:75], v[14:15] op_sel_hi:[1,0,1] clamp
	v_pk_fma_f32 v[98:99], v[98:99], s[64:65], v[186:187] op_sel_hi:[1,0,0]
	v_pk_fma_f32 v[102:103], v[102:103], s[96:97], s[96:97] op_sel_hi:[1,0,0]
	v_rcp_f32_e32 v102, v102
	v_rcp_f32_e32 v103, v103
	v_pk_fma_f32 v[104:105], v[104:105], s[96:97], s[96:97] op_sel_hi:[1,0,0]
	v_pk_mul_f32 v[32:33], v[32:33], v[98:99]
	v_rcp_f32_e32 v104, v104
	v_rcp_f32_e32 v105, v105
	v_pk_mul_f32 v[32:33], v[32:33], v[102:103]
	v_pk_fma_f32 v[100:101], v[100:101], s[74:75], v[12:13] op_sel_hi:[1,0,1] clamp
	v_cvt_pk_fp8_f32 v31, v32, v33
	v_pk_fma_f32 v[100:101], v[100:101], s[64:65], v[186:187] op_sel_hi:[1,0,0]
	v_pk_mul_f32 v[26:27], v[26:27], v[100:101]
	v_and_b32_e32 v25, 16, v25
	v_pk_mul_f32 v[26:27], v[26:27], v[104:105]
	s_sub_i32 s38, s38, s35
	v_cvt_pk_fp8_f32 v31, v26, v27 op_sel:[0,0,1]
	v_or_b32_e32 v26, v24, v25
	v_ashrrev_i32_e32 v27, 31, v26
	v_lshlrev_b64 v[26:27], 10, v[26:27]
	s_ashr_i32 s39, s38, 31
	v_lshl_add_u64 v[26:27], s[12:13], 0, v[26:27]
	v_lshl_add_u64 v[26:27], v[26:27], 0, s[38:39]
	v_mov_b32_e32 v7, v163
	v_lshl_add_u64 v[26:27], v[26:27], 0, v[162:163]
	v_permlane16_swap_b32_e32 v2, v4
	v_permlane16_swap_b32_e32 v3, v5
	v_lshl_add_u64 v[26:27], v[26:27], 0, v[6:7]
	global_store_dwordx4 v[26:27], v[2:5], off
	v_or_b32_e32 v26, 32, v25
	v_permlane16_swap_b32_e32 v28, v30
	v_or_b32_e32 v2, v24, v26
	v_ashrrev_i32_e32 v3, 31, v2
	v_lshlrev_b64 v[2:3], 10, v[2:3]
	v_lshl_add_u64 v[2:3], s[12:13], 0, v[2:3]
	v_lshl_add_u64 v[2:3], v[2:3], 0, s[38:39]
	v_lshl_add_u64 v[2:3], v[2:3], 0, v[162:163]
	v_permlane16_swap_b32_e32 v29, v31
	v_lshl_add_u64 v[2:3], v[2:3], 0, v[6:7]
	v_pk_fma_f32 v[4:5], v[94:95], s[98:99], v[18:19] op_sel_hi:[1,0,1]
	global_store_dwordx4 v[2:3], v[28:31], off
	v_pk_fma_f32 v[2:3], v[96:97], s[98:99], v[16:17] op_sel_hi:[1,0,1]
	v_max_f32_e32 v4, 0xc1898193, v4
	v_max_f32_e32 v5, 0xc1898193, v5
	v_max_f32_e32 v32, 0xc1898193, v2
	v_max_f32_e32 v33, 0xc1898193, v3
	v_exp_f32_e32 v2, v4
	v_exp_f32_e32 v3, v5
	v_pk_fma_f32 v[30:31], v[90:91], s[74:75], v[22:23] op_sel_hi:[1,0,1] clamp
	v_exp_f32_e32 v90, v32
	v_exp_f32_e32 v91, v33
	v_pk_fma_f32 v[2:3], v[2:3], s[96:97], s[96:97] op_sel_hi:[1,0,0]
	v_pk_fma_f32 v[30:31], v[30:31], s[64:65], v[186:187] op_sel_hi:[1,0,0]
	v_rcp_f32_e32 v2, v2
	v_rcp_f32_e32 v3, v3
	v_pk_fma_f32 v[28:29], v[92:93], s[74:75], v[20:21] op_sel_hi:[1,0,1] clamp
	v_pk_fma_f32 v[90:91], v[90:91], s[96:97], s[96:97] op_sel_hi:[1,0,0]
	v_pk_mul_f32 v[4:5], v[4:5], v[30:31]
	v_pk_fma_f32 v[28:29], v[28:29], s[64:65], v[186:187] op_sel_hi:[1,0,0]
	v_rcp_f32_e32 v90, v90
	v_rcp_f32_e32 v91, v91
	v_pk_mul_f32 v[4:5], v[4:5], v[2:3]
	v_cvt_pk_fp8_f32 v2, v4, v5
	v_pk_mul_f32 v[4:5], v[32:33], v[28:29]
	v_pk_fma_f32 v[28:29], v[86:87], s[98:99], v[10:11] op_sel_hi:[1,0,1]
	v_pk_mul_f32 v[4:5], v[4:5], v[90:91]
	v_max_f32_e32 v28, 0xc1898193, v28
	v_max_f32_e32 v29, 0xc1898193, v29
	v_pk_fma_f32 v[32:33], v[82:83], s[74:75], v[14:15] op_sel_hi:[1,0,1] clamp
	v_exp_f32_e32 v82, v28
	v_cvt_pk_fp8_f32 v2, v4, v5 op_sel:[0,0,1]
	v_pk_fma_f32 v[4:5], v[88:89], s[98:99], v[8:9] op_sel_hi:[1,0,1]
	v_exp_f32_e32 v83, v29
	v_max_f32_e32 v4, 0xc1898193, v4
	v_max_f32_e32 v5, 0xc1898193, v5
	v_pk_fma_f32 v[30:31], v[84:85], s[74:75], v[12:13] op_sel_hi:[1,0,1] clamp
	v_exp_f32_e32 v84, v4
	v_exp_f32_e32 v85, v5
	v_pk_fma_f32 v[82:83], v[82:83], s[96:97], s[96:97] op_sel_hi:[1,0,0]
	v_pk_fma_f32 v[32:33], v[32:33], s[64:65], v[186:187] op_sel_hi:[1,0,0]
	v_rcp_f32_e32 v82, v82
	v_rcp_f32_e32 v83, v83
	v_pk_fma_f32 v[84:85], v[84:85], s[96:97], s[96:97] op_sel_hi:[1,0,0]
	v_pk_mul_f32 v[28:29], v[28:29], v[32:33]
	v_rcp_f32_e32 v84, v84
	v_rcp_f32_e32 v85, v85
	v_pk_mul_f32 v[28:29], v[28:29], v[82:83]
	v_cvt_pk_fp8_f32 v3, v28, v29
	v_pk_fma_f32 v[30:31], v[30:31], s[64:65], v[186:187] op_sel_hi:[1,0,0]
	v_pk_mul_f32 v[4:5], v[4:5], v[30:31]
	v_pk_fma_f32 v[28:29], v[78:79], s[98:99], v[18:19] op_sel_hi:[1,0,1]
	v_pk_mul_f32 v[4:5], v[4:5], v[84:85]
	v_max_f32_e32 v28, 0xc1898193, v28
	v_cvt_pk_fp8_f32 v3, v4, v5 op_sel:[0,0,1]
	v_pk_fma_f32 v[4:5], v[80:81], s[98:99], v[16:17] op_sel_hi:[1,0,1]
	v_max_f32_e32 v29, 0xc1898193, v29
	v_pk_fma_f32 v[32:33], v[74:75], s[74:75], v[22:23] op_sel_hi:[1,0,1] clamp
	v_max_f32_e32 v74, 0xc1898193, v4
	v_max_f32_e32 v75, 0xc1898193, v5
	v_exp_f32_e32 v4, v28
	v_exp_f32_e32 v5, v29
	v_pk_fma_f32 v[30:31], v[76:77], s[74:75], v[20:21] op_sel_hi:[1,0,1] clamp
	v_exp_f32_e32 v76, v74
	v_exp_f32_e32 v77, v75
	v_pk_fma_f32 v[4:5], v[4:5], s[96:97], s[96:97] op_sel_hi:[1,0,0]
	v_pk_fma_f32 v[32:33], v[32:33], s[64:65], v[186:187] op_sel_hi:[1,0,0]
	v_rcp_f32_e32 v4, v4
	v_rcp_f32_e32 v5, v5
	v_pk_fma_f32 v[76:77], v[76:77], s[96:97], s[96:97] op_sel_hi:[1,0,0]
	v_pk_mul_f32 v[28:29], v[28:29], v[32:33]
	v_pk_fma_f32 v[30:31], v[30:31], s[64:65], v[186:187] op_sel_hi:[1,0,0]
	v_rcp_f32_e32 v76, v76
	v_rcp_f32_e32 v77, v77
	v_pk_mul_f32 v[28:29], v[28:29], v[4:5]
	v_cvt_pk_fp8_f32 v4, v28, v29
	v_pk_mul_f32 v[28:29], v[74:75], v[30:31]
	v_pk_fma_f32 v[30:31], v[70:71], s[98:99], v[10:11] op_sel_hi:[1,0,1]
	v_pk_mul_f32 v[28:29], v[28:29], v[76:77]
	v_max_f32_e32 v30, 0xc1898193, v30
	v_max_f32_e32 v31, 0xc1898193, v31
	v_pk_fma_f32 v[32:33], v[68:69], s[74:75], v[12:13] op_sel_hi:[1,0,1] clamp
	v_exp_f32_e32 v68, v30
	v_cvt_pk_fp8_f32 v4, v28, v29 op_sel:[0,0,1]
	v_pk_fma_f32 v[28:29], v[72:73], s[98:99], v[8:9] op_sel_hi:[1,0,1]
	v_exp_f32_e32 v69, v31
	v_max_f32_e32 v28, 0xc1898193, v28
	v_max_f32_e32 v29, 0xc1898193, v29
	v_exp_f32_e32 v70, v28
	v_exp_f32_e32 v71, v29
	v_pk_fma_f32 v[68:69], v[68:69], s[96:97], s[96:97] op_sel_hi:[1,0,0]
	v_pk_fma_f32 v[66:67], v[66:67], s[74:75], v[14:15] op_sel_hi:[1,0,1] clamp
	v_rcp_f32_e32 v68, v68
	v_rcp_f32_e32 v69, v69
	v_pk_fma_f32 v[66:67], v[66:67], s[64:65], v[186:187] op_sel_hi:[1,0,0]
	v_pk_fma_f32 v[70:71], v[70:71], s[96:97], s[96:97] op_sel_hi:[1,0,0]
	v_pk_mul_f32 v[30:31], v[30:31], v[66:67]
	v_rcp_f32_e32 v70, v70
	v_rcp_f32_e32 v71, v71
	v_pk_mul_f32 v[30:31], v[30:31], v[68:69]
	v_cvt_pk_fp8_f32 v5, v30, v31
	v_pk_fma_f32 v[32:33], v[32:33], s[64:65], v[186:187] op_sel_hi:[1,0,0]
	v_pk_mul_f32 v[28:29], v[28:29], v[32:33]
	v_pk_fma_f32 v[30:31], v[62:63], s[98:99], v[18:19] op_sel_hi:[1,0,1]
	v_pk_mul_f32 v[28:29], v[28:29], v[70:71]
	v_pk_fma_f32 v[32:33], v[60:61], s[74:75], v[20:21] op_sel_hi:[1,0,1] clamp
	v_cvt_pk_fp8_f32 v5, v28, v29 op_sel:[0,0,1]
	v_pk_fma_f32 v[28:29], v[64:65], s[98:99], v[16:17] op_sel_hi:[1,0,1]
	v_max_f32_e32 v30, 0xc1898193, v30
	v_max_f32_e32 v60, 0xc1898193, v28
	v_max_f32_e32 v31, 0xc1898193, v31
	v_max_f32_e32 v61, 0xc1898193, v29
	v_exp_f32_e32 v28, v30
	v_exp_f32_e32 v62, v60
	v_exp_f32_e32 v63, v61
	v_exp_f32_e32 v29, v31
	v_pk_fma_f32 v[58:59], v[58:59], s[74:75], v[22:23] op_sel_hi:[1,0,1] clamp
	v_pk_fma_f32 v[32:33], v[32:33], s[64:65], v[186:187] op_sel_hi:[1,0,0]
	v_pk_fma_f32 v[58:59], v[58:59], s[64:65], v[186:187] op_sel_hi:[1,0,0]
	v_pk_fma_f32 v[28:29], v[28:29], s[96:97], s[96:97] op_sel_hi:[1,0,0]
	v_rcp_f32_e32 v28, v28
	v_rcp_f32_e32 v29, v29
	v_pk_fma_f32 v[62:63], v[62:63], s[96:97], s[96:97] op_sel_hi:[1,0,0]
	v_pk_mul_f32 v[30:31], v[30:31], v[58:59]
	v_rcp_f32_e32 v62, v62
	v_rcp_f32_e32 v63, v63
	v_pk_mul_f32 v[30:31], v[30:31], v[28:29]
	v_cvt_pk_fp8_f32 v28, v30, v31
	v_pk_mul_f32 v[30:31], v[60:61], v[32:33]
	v_pk_fma_f32 v[32:33], v[54:55], s[98:99], v[10:11] op_sel_hi:[1,0,1]
	v_pk_mul_f32 v[30:31], v[30:31], v[62:63]
	v_max_f32_e32 v32, 0xc1898193, v32
	v_max_f32_e32 v33, 0xc1898193, v33
	v_exp_f32_e32 v54, v32
	v_cvt_pk_fp8_f32 v28, v30, v31 op_sel:[0,0,1]
	v_pk_fma_f32 v[30:31], v[56:57], s[98:99], v[8:9] op_sel_hi:[1,0,1]
	v_exp_f32_e32 v55, v33
	v_max_f32_e32 v30, 0xc1898193, v30
	v_max_f32_e32 v31, 0xc1898193, v31
	v_exp_f32_e32 v56, v30
	v_exp_f32_e32 v57, v31
	v_pk_fma_f32 v[54:55], v[54:55], s[96:97], s[96:97] op_sel_hi:[1,0,0]
	v_pk_fma_f32 v[50:51], v[50:51], s[74:75], v[14:15] op_sel_hi:[1,0,1] clamp
	v_rcp_f32_e32 v54, v54
	v_rcp_f32_e32 v55, v55
	v_pk_fma_f32 v[50:51], v[50:51], s[64:65], v[186:187] op_sel_hi:[1,0,0]
	v_pk_fma_f32 v[56:57], v[56:57], s[96:97], s[96:97] op_sel_hi:[1,0,0]
	v_pk_mul_f32 v[32:33], v[32:33], v[50:51]
	v_rcp_f32_e32 v56, v56
	v_rcp_f32_e32 v57, v57
	v_pk_mul_f32 v[32:33], v[32:33], v[54:55]
	v_pk_fma_f32 v[52:53], v[52:53], s[74:75], v[12:13] op_sel_hi:[1,0,1] clamp
	v_cvt_pk_fp8_f32 v29, v32, v33
	v_pk_fma_f32 v[52:53], v[52:53], s[64:65], v[186:187] op_sel_hi:[1,0,0]
	v_pk_mul_f32 v[30:31], v[30:31], v[52:53]
	v_pk_fma_f32 v[16:17], v[48:49], s[98:99], v[16:17] op_sel_hi:[1,0,1]
	v_pk_fma_f32 v[18:19], v[46:47], s[98:99], v[18:19] op_sel_hi:[1,0,1]
	v_pk_mul_f32 v[30:31], v[30:31], v[56:57]
	v_max_f32_e32 v18, 0xc1898193, v18
	v_max_f32_e32 v16, 0xc1898193, v16
	v_cvt_pk_fp8_f32 v29, v30, v31 op_sel:[0,0,1]
	v_max_f32_e32 v19, 0xc1898193, v19
	v_max_f32_e32 v17, 0xc1898193, v17
	v_exp_f32_e32 v30, v18
	v_exp_f32_e32 v32, v16
	v_exp_f32_e32 v33, v17
	v_exp_f32_e32 v31, v19
	v_pk_fma_f32 v[22:23], v[42:43], s[74:75], v[22:23] op_sel_hi:[1,0,1] clamp
	v_pk_fma_f32 v[20:21], v[44:45], s[74:75], v[20:21] op_sel_hi:[1,0,1] clamp
	v_pk_fma_f32 v[22:23], v[22:23], s[64:65], v[186:187] op_sel_hi:[1,0,0]
	v_pk_fma_f32 v[30:31], v[30:31], s[96:97], s[96:97] op_sel_hi:[1,0,0]
	v_rcp_f32_e32 v30, v30
	v_rcp_f32_e32 v31, v31
	v_pk_fma_f32 v[32:33], v[32:33], s[96:97], s[96:97] op_sel_hi:[1,0,0]
	v_pk_mul_f32 v[18:19], v[18:19], v[22:23]
	v_rcp_f32_e32 v32, v32
	v_rcp_f32_e32 v33, v33
	v_pk_mul_f32 v[18:19], v[18:19], v[30:31]
	v_cvt_pk_fp8_f32 v30, v18, v19
	v_pk_fma_f32 v[20:21], v[20:21], s[64:65], v[186:187] op_sel_hi:[1,0,0]
	v_pk_mul_f32 v[16:17], v[16:17], v[20:21]
	v_pk_fma_f32 v[10:11], v[38:39], s[98:99], v[10:11] op_sel_hi:[1,0,1]
	v_pk_mul_f32 v[16:17], v[16:17], v[32:33]
	v_max_f32_e32 v10, 0xc1898193, v10
	v_max_f32_e32 v11, 0xc1898193, v11
	v_cvt_pk_fp8_f32 v30, v16, v17 op_sel:[0,0,1]
	v_exp_f32_e32 v16, v10
	v_exp_f32_e32 v17, v11
	v_pk_fma_f32 v[8:9], v[40:41], s[98:99], v[8:9] op_sel_hi:[1,0,1]
	v_pk_fma_f32 v[14:15], v[34:35], s[74:75], v[14:15] op_sel_hi:[1,0,1] clamp
	v_max_f32_e32 v8, 0xc1898193, v8
	v_max_f32_e32 v9, 0xc1898193, v9
	v_exp_f32_e32 v18, v8
	v_exp_f32_e32 v19, v9
	v_pk_fma_f32 v[16:17], v[16:17], s[96:97], s[96:97] op_sel_hi:[1,0,0]
	v_pk_fma_f32 v[14:15], v[14:15], s[64:65], v[186:187] op_sel_hi:[1,0,0]
	v_rcp_f32_e32 v16, v16
	v_rcp_f32_e32 v17, v17
	v_pk_fma_f32 v[18:19], v[18:19], s[96:97], s[96:97] op_sel_hi:[1,0,0]
	v_pk_mul_f32 v[10:11], v[10:11], v[14:15]
	v_rcp_f32_e32 v18, v18
	v_rcp_f32_e32 v19, v19
	v_pk_mul_f32 v[10:11], v[10:11], v[16:17]
	v_pk_fma_f32 v[12:13], v[36:37], s[74:75], v[12:13] op_sel_hi:[1,0,1] clamp
	v_cvt_pk_fp8_f32 v31, v10, v11
	v_pk_fma_f32 v[12:13], v[12:13], s[64:65], v[186:187] op_sel_hi:[1,0,0]
	v_pk_mul_f32 v[8:9], v[8:9], v[12:13]
	v_add_u32_e32 v10, 0x80, v24
	v_pk_mul_f32 v[8:9], v[8:9], v[18:19]
	v_permlane16_swap_b32_e32 v2, v4
	v_cvt_pk_fp8_f32 v31, v8, v9 op_sel:[0,0,1]
	v_or_b32_e32 v8, v10, v25
	v_ashrrev_i32_e32 v9, 31, v8
	v_lshlrev_b64 v[8:9], 10, v[8:9]
	v_lshl_add_u64 v[8:9], s[12:13], 0, v[8:9]
	v_lshl_add_u64 v[8:9], v[8:9], 0, s[38:39]
	v_lshl_add_u64 v[8:9], v[8:9], 0, v[162:163]
	v_permlane16_swap_b32_e32 v3, v5
	v_lshl_add_u64 v[8:9], v[8:9], 0, v[6:7]
	global_store_dwordx4 v[8:9], v[2:5], off
	v_permlane16_swap_b32_e32 v28, v30
	s_nop 0
	v_or_b32_e32 v2, v10, v26
	v_ashrrev_i32_e32 v3, 31, v2
	v_lshlrev_b64 v[2:3], 10, v[2:3]
	v_lshl_add_u64 v[2:3], s[12:13], 0, v[2:3]
	v_lshl_add_u64 v[2:3], v[2:3], 0, s[38:39]
	v_lshl_add_u64 v[2:3], v[2:3], 0, v[162:163]
	v_permlane16_swap_b32_e32 v29, v31
	v_lshl_add_u64 v[2:3], v[2:3], 0, v[6:7]
	s_and_b64 vcc, exec, s[4:5]
	s_mov_b64 s[4:5], -1
	global_store_dwordx4 v[2:3], v[28:31], off
	s_cbranch_vccnz .LBB0_557
	s_andn2_b64 vcc, exec, s[16:17]
	s_cbranch_vccnz .LBB0_569
	s_lshl_b32 s4, s66, 10
	s_and_b32 s4, s4, 0x400
	s_add_i32 s4, s4, 0
	s_ashr_i32 s37, s36, 31
	s_add_i32 s35, s4, 0x24cc0
	s_lshl_b64 s[4:5], s[36:37], 13
	s_add_u32 s37, s14, s4
	s_addc_u32 s38, s15, s5
	s_lshl_b32 s4, s36, 10
	s_lshl_b32 s5, s34, 7
	s_sub_i32 s4, s5, s4
	s_ashr_i32 s5, s4, 31
	s_lshl_b64 s[4:5], s[4:5], 2
	s_add_u32 s4, s37, s4
	s_addc_u32 s5, s38, s5
	s_mov_b32 m0, s35
	s_nop 0
	global_load_lds_dwordx4 v178, s[4:5] offset:0
